# nt (streaming) hint on the 16 in-projection GEMM output stores so the dirty output leaves L2 before the phase barrier
# baseline (speedup 1.0000x reference)
; __device__ __forceinline__ unsigned cvt_pk_bf16(float lo, float hi) { unsigned r; asm volatile("v_cvt_pk_bf16_f32 %0, %1, %2" : "=v"(r) : "v"(lo), "v"(hi)); return r; }
; __device__ __forceinline__ int fresh_lane() { unsigned z = 0u; asm volatile("" : "+v"(z)); return (int)__builtin_amdgcn_mbcnt_hi(~0u, __builtin_amdgcn_mbcnt_lo(~0u, z)); }
;     __device__ __forceinline__ void operator()(const pg8::f32x4 (&acc)[2][2][4][2], const pg8::Unit& u, int wr, int wc, int fr_, int fq_) const {
;         const int el_ = fresh_lane(), fr = el_ & 15, fq = el_ >> 4; (void)fr_; (void)fq_;
;         const int row0 = u.pm * 256 + wr * 64 + fr, col0 = u.pn * 256 + wc * 32 + 8 * fq;
;         const __amdgpu_buffer_rsrc_t rs = __builtin_amdgcn_make_buffer_rsrc((void*)O, (short)0, (int)((size_t)T * ldc * 2), 0x00020000);
;         float sxv[8];
; #pragma unroll
;         for (int r8 = 0; r8 < 8; ++r8) sxv[r8] = SX[row0 + (r8 >> 2) * 128 + (r8 & 3) * 16];
; #pragma unroll
;         for (int bj = 0; bj < 2; ++bj) {
;             const pg8::f32x4 s0 = *(const pg8::f32x4*)(SW + col0 + bj * 128), s1 = *(const pg8::f32x4*)(SW + col0 + bj * 128 + 4);
; #pragma unroll
;             for (int ai = 0; ai < 2; ++ai)
; #pragma unroll
;                 for (int m = 0; m < 4; ++m) { const int row = row0 + ai * 128 + m * 16; const float sx = sxv[ai * 4 + m];
;                     const unsigned ro = (unsigned)(((size_t)row * ldc + col0) * 2);
;                     const pg8::f32x4 a0 = acc[ai][bj][m][0], a1 = acc[ai][bj][m][1];
;                     typedef int i32x4_ __attribute__((ext_vector_type(4)));
;                     const pg8::f32x4 f0 = __builtin_convertvector(__builtin_bit_cast(i32x4_, a0), pg8::f32x4) * (s0 * sx), f1 = __builtin_convertvector(__builtin_bit_cast(i32x4_, a1), pg8::f32x4) * (s1 * sx);
;                     const float v[8] = {f0[0], f0[1], f0[2], f0[3], f1[0], f1[1], f1[2], f1[3]};
;                     v4u w; w.x = pg8::cvt_pk_bf16(v[0], v[1]); w.y = pg8::cvt_pk_bf16(v[2], v[3]); w.z = pg8::cvt_pk_bf16(v[4], v[5]); w.w = pg8::cvt_pk_bf16(v[6], v[7]);
;                     __builtin_amdgcn_raw_buffer_store_b128(w, rs, ro + bj * 256, 0, 0); }
.LBB0_288:
	v_mov_b32_e32 v0, v1
	s_lshl_b32 s15, s22, 8
	v_mbcnt_lo_u32_b32 v0, -1, v0
	v_mbcnt_hi_u32_b32 v0, -1, v0
	s_add_i32 s15, s15, s56
	v_and_or_b32 v154, v0, 15, s15
	v_ashrrev_i32_e32 v0, 1, v0
	s_lshl_b32 s15, s23, 8
	v_and_b32_e32 v108, -8, v0
	s_or_b32 s15, s15, s57
	v_add_u32_e32 v156, s15, v108
	v_ashrrev_i32_e32 v155, 31, v154
	v_ashrrev_i32_e32 v157, 31, v156
	v_lshl_add_u64 v[106:107], v[154:155], 2, s[8:9]
	v_lshl_add_u64 v[152:153], v[156:157], 2, s[10:11]
	global_load_dword v150, v[106:107], off
	global_load_dword v148, v[106:107], off offset:64
	global_load_dword v146, v[106:107], off offset:128
	global_load_dword v144, v[106:107], off offset:192
	global_load_dword v142, v[106:107], off offset:512
	global_load_dword v140, v[106:107], off offset:576
	global_load_dword v138, v[106:107], off offset:640
	global_load_dword v0, v[106:107], off offset:704
	s_nop 0
	global_load_dwordx4 v[106:109], v[152:153], off offset:16
	global_load_dwordx4 v[110:113], v[152:153], off
	s_movk_i32 s15, 0x1800
	v_cvt_f32_i32_e32 v135, v135
	v_cvt_f32_i32_e32 v134, v134
	v_cvt_f32_i32_e32 v137, v137
	v_cvt_f32_i32_e32 v136, v136
	v_mul_lo_u32 v151, v154, s15
	v_cvt_f32_i32_e32 v131, v131
	v_cvt_f32_i32_e32 v130, v130
	v_cvt_f32_i32_e32 v133, v133
	v_cvt_f32_i32_e32 v132, v132
	v_add_lshl_u32 v151, v156, v151, 1
	v_cvt_f32_i32_e32 v127, v127
	v_cvt_f32_i32_e32 v126, v126
	v_cvt_f32_i32_e32 v129, v129
	v_cvt_f32_i32_e32 v128, v128
	v_cvt_f32_i32_e32 v123, v123
	v_cvt_f32_i32_e32 v122, v122
	v_cvt_f32_i32_e32 v125, v125
	v_cvt_f32_i32_e32 v124, v124
	v_cvt_f32_i32_e32 v119, v119
	v_cvt_f32_i32_e32 v118, v118
	v_cvt_f32_i32_e32 v121, v121
	v_cvt_f32_i32_e32 v120, v120
	v_cvt_f32_i32_e32 v115, v115
	v_cvt_f32_i32_e32 v114, v114
	v_cvt_f32_i32_e32 v117, v117
	v_cvt_f32_i32_e32 v116, v116
	v_cvt_f32_i32_e32 v103, v103
	v_cvt_f32_i32_e32 v102, v102
	v_cvt_f32_i32_e32 v105, v105
	v_cvt_f32_i32_e32 v104, v104
	v_cvt_f32_i32_e32 v99, v99
	v_cvt_f32_i32_e32 v98, v98
	v_cvt_f32_i32_e32 v101, v101
	v_cvt_f32_i32_e32 v100, v100
	v_cvt_f32_i32_e32 v95, v95
	v_cvt_f32_i32_e32 v94, v94
	v_cvt_f32_i32_e32 v97, v97
	v_cvt_f32_i32_e32 v96, v96
	v_cvt_f32_i32_e32 v91, v91
	v_cvt_f32_i32_e32 v90, v90
	v_cvt_f32_i32_e32 v93, v93
	v_cvt_f32_i32_e32 v92, v92
	v_cvt_f32_i32_e32 v87, v87
	v_cvt_f32_i32_e32 v86, v86
	v_cvt_f32_i32_e32 v89, v89
	v_cvt_f32_i32_e32 v88, v88
	v_cvt_f32_i32_e32 v83, v83
	v_cvt_f32_i32_e32 v82, v82
	v_cvt_f32_i32_e32 v85, v85
	v_cvt_f32_i32_e32 v84, v84
	v_cvt_f32_i32_e32 v79, v79
	v_cvt_f32_i32_e32 v78, v78
	v_cvt_f32_i32_e32 v81, v81
	v_cvt_f32_i32_e32 v80, v80
	v_cvt_f32_i32_e32 v75, v75
	v_cvt_f32_i32_e32 v74, v74
	v_cvt_f32_i32_e32 v77, v77
	v_cvt_f32_i32_e32 v76, v76
	v_cvt_f32_i32_e32 v71, v71
	v_cvt_f32_i32_e32 v70, v70
	v_cvt_f32_i32_e32 v73, v73
	v_cvt_f32_i32_e32 v72, v72
	v_cvt_f32_i32_e32 v67, v67
	v_cvt_f32_i32_e32 v66, v66
	v_cvt_f32_i32_e32 v69, v69
	v_cvt_f32_i32_e32 v68, v68
	v_cvt_f32_i32_e32 v63, v63
	v_cvt_f32_i32_e32 v62, v62
	v_cvt_f32_i32_e32 v65, v65
	v_cvt_f32_i32_e32 v64, v64
	v_cvt_f32_i32_e32 v59, v59
	v_cvt_f32_i32_e32 v58, v58
	v_cvt_f32_i32_e32 v61, v61
	v_cvt_f32_i32_e32 v60, v60
	v_cvt_f32_i32_e32 v55, v55
	v_cvt_f32_i32_e32 v54, v54
	v_cvt_f32_i32_e32 v57, v57
	v_cvt_f32_i32_e32 v56, v56
	s_waitcnt vmcnt(0)
	v_pk_mul_f32 v[154:155], v[150:151], v[110:111] op_sel_hi:[0,1]
	v_pk_mul_f32 v[156:157], v[150:151], v[112:113] op_sel_hi:[0,1]
	v_pk_mul_f32 v[136:137], v[156:157], v[136:137]
	v_pk_mul_f32 v[134:135], v[154:155], v[134:135]
	v_pk_mul_f32 v[154:155], v[150:151], v[106:107] op_sel_hi:[0,1]
	v_pk_mul_f32 v[156:157], v[150:151], v[108:109] op_sel_hi:[0,1]
	v_pk_mul_f32 v[156:157], v[156:157], v[132:133]
	v_pk_mul_f32 v[132:133], v[154:155], v[130:131]
	v_cvt_pk_bf16_f32 v130, v134, v135
	v_cvt_pk_bf16_f32 v131, v136, v137
	v_pk_mul_f32 v[134:135], v[148:149], v[112:113] op_sel_hi:[0,1]
	v_cvt_pk_bf16_f32 v132, v132, v133
	v_cvt_pk_bf16_f32 v133, v156, v157
	buffer_store_dwordx4 v[130:133], v151, s[36:39], 0 offen nt
	v_pk_mul_f32 v[128:129], v[134:135], v[128:129]
	v_pk_mul_f32 v[134:135], v[148:149], v[108:109] op_sel_hi:[0,1]
	v_pk_mul_f32 v[132:133], v[148:149], v[110:111] op_sel_hi:[0,1]
	v_pk_mul_f32 v[126:127], v[132:133], v[126:127]
	v_pk_mul_f32 v[132:133], v[148:149], v[106:107] op_sel_hi:[0,1]
	v_pk_mul_f32 v[134:135], v[134:135], v[124:125]
	v_pk_mul_f32 v[124:125], v[132:133], v[122:123]
	v_add_u32_e32 v130, 0x30000, v151
	v_cvt_pk_bf16_f32 v122, v126, v127
	v_cvt_pk_bf16_f32 v123, v128, v129
	v_cvt_pk_bf16_f32 v124, v124, v125
	v_cvt_pk_bf16_f32 v125, v134, v135
	buffer_store_dwordx4 v[122:125], v130, s[36:39], 0 offen nt
	v_pk_mul_f32 v[126:127], v[146:147], v[112:113] op_sel_hi:[0,1]
	v_pk_mul_f32 v[120:121], v[126:127], v[120:121]
	v_pk_mul_f32 v[124:125], v[146:147], v[110:111] op_sel_hi:[0,1]
	v_pk_mul_f32 v[118:119], v[124:125], v[118:119]
	v_pk_mul_f32 v[124:125], v[146:147], v[106:107] op_sel_hi:[0,1]
	v_pk_mul_f32 v[126:127], v[146:147], v[108:109] op_sel_hi:[0,1]
	v_pk_mul_f32 v[126:127], v[126:127], v[116:117]
	v_pk_mul_f32 v[116:117], v[124:125], v[114:115]
	v_add_u32_e32 v122, 0x60000, v151
	v_cvt_pk_bf16_f32 v114, v118, v119
	v_cvt_pk_bf16_f32 v115, v120, v121
	v_cvt_pk_bf16_f32 v116, v116, v117
	v_cvt_pk_bf16_f32 v117, v126, v127
	buffer_store_dwordx4 v[114:117], v122, s[36:39], 0 offen nt
	v_pk_mul_f32 v[118:119], v[144:145], v[112:113] op_sel_hi:[0,1]
	v_pk_mul_f32 v[104:105], v[118:119], v[104:105]
	v_pk_mul_f32 v[116:117], v[144:145], v[110:111] op_sel_hi:[0,1]
	v_pk_mul_f32 v[102:103], v[116:117], v[102:103]
	v_pk_mul_f32 v[116:117], v[144:145], v[106:107] op_sel_hi:[0,1]
; __device__ __forceinline__ unsigned cvt_pk_bf16(float lo, float hi) { unsigned r; asm volatile("v_cvt_pk_bf16_f32 %0, %1, %2" : "=v"(r) : "v"(lo), "v"(hi)); return r; }
;     __device__ __forceinline__ void operator()(const pg8::f32x4 (&acc)[2][2][4][2], const pg8::Unit& u, int wr, int wc, int fr_, int fq_) const {
;     ...
;         for (int bj = 0; bj < 2; ++bj) {
;             const pg8::f32x4 s0 = *(const pg8::f32x4*)(SW + col0 + bj * 128), s1 = *(const pg8::f32x4*)(SW + col0 + bj * 128 + 4);
; #pragma unroll
;             for (int ai = 0; ai < 2; ++ai)
; #pragma unroll
;                 for (int m = 0; m < 4; ++m) { const int row = row0 + ai * 128 + m * 16; const float sx = sxv[ai * 4 + m];
;                     const unsigned ro = (unsigned)(((size_t)row * ldc + col0) * 2);
;                     const pg8::f32x4 a0 = acc[ai][bj][m][0], a1 = acc[ai][bj][m][1];
;                     typedef int i32x4_ __attribute__((ext_vector_type(4)));
;                     const pg8::f32x4 f0 = __builtin_convertvector(__builtin_bit_cast(i32x4_, a0), pg8::f32x4) * (s0 * sx), f1 = __builtin_convertvector(__builtin_bit_cast(i32x4_, a1), pg8::f32x4) * (s1 * sx);
;                     const float v[8] = {f0[0], f0[1], f0[2], f0[3], f1[0], f1[1], f1[2], f1[3]};
;                     v4u w; w.x = pg8::cvt_pk_bf16(v[0], v[1]); w.y = pg8::cvt_pk_bf16(v[2], v[3]); w.z = pg8::cvt_pk_bf16(v[4], v[5]); w.w = pg8::cvt_pk_bf16(v[6], v[7]);
;                     __builtin_amdgcn_raw_buffer_store_b128(w, rs, ro + bj * 256, 0, 0); }
	v_pk_mul_f32 v[118:119], v[144:145], v[108:109] op_sel_hi:[0,1]
	v_pk_mul_f32 v[118:119], v[118:119], v[100:101]
	v_pk_mul_f32 v[100:101], v[116:117], v[98:99]
	v_add_u32_e32 v114, 0x90000, v151
	v_cvt_pk_bf16_f32 v98, v102, v103
	v_cvt_pk_bf16_f32 v99, v104, v105
	v_cvt_pk_bf16_f32 v100, v100, v101
	v_cvt_pk_bf16_f32 v101, v118, v119
	buffer_store_dwordx4 v[98:101], v114, s[36:39], 0 offen nt
	v_pk_mul_f32 v[102:103], v[142:143], v[112:113] op_sel_hi:[0,1]
	v_pk_mul_f32 v[96:97], v[102:103], v[96:97]
	v_pk_mul_f32 v[100:101], v[142:143], v[110:111] op_sel_hi:[0,1]
	v_pk_mul_f32 v[94:95], v[100:101], v[94:95]
	v_pk_mul_f32 v[100:101], v[142:143], v[106:107] op_sel_hi:[0,1]
	v_pk_mul_f32 v[102:103], v[142:143], v[108:109] op_sel_hi:[0,1]
	v_pk_mul_f32 v[102:103], v[102:103], v[92:93]
	v_pk_mul_f32 v[92:93], v[100:101], v[90:91]
	v_add_u32_e32 v98, 0x180000, v151
	v_cvt_pk_bf16_f32 v90, v94, v95
	v_cvt_pk_bf16_f32 v91, v96, v97
	v_cvt_pk_bf16_f32 v92, v92, v93
	v_cvt_pk_bf16_f32 v93, v102, v103
	buffer_store_dwordx4 v[90:93], v98, s[36:39], 0 offen nt
	v_pk_mul_f32 v[94:95], v[140:141], v[112:113] op_sel_hi:[0,1]
	v_pk_mul_f32 v[88:89], v[94:95], v[88:89]
	v_pk_mul_f32 v[92:93], v[140:141], v[110:111] op_sel_hi:[0,1]
	v_pk_mul_f32 v[86:87], v[92:93], v[86:87]
	v_pk_mul_f32 v[92:93], v[140:141], v[106:107] op_sel_hi:[0,1]
	v_pk_mul_f32 v[94:95], v[140:141], v[108:109] op_sel_hi:[0,1]
	v_pk_mul_f32 v[94:95], v[94:95], v[84:85]
	v_pk_mul_f32 v[84:85], v[92:93], v[82:83]
	v_add_u32_e32 v90, 0x1b0000, v151
	v_cvt_pk_bf16_f32 v82, v86, v87
	v_cvt_pk_bf16_f32 v83, v88, v89
	v_cvt_pk_bf16_f32 v84, v84, v85
	v_cvt_pk_bf16_f32 v85, v94, v95
	buffer_store_dwordx4 v[82:85], v90, s[36:39], 0 offen nt
	v_pk_mul_f32 v[86:87], v[138:139], v[112:113] op_sel_hi:[0,1]
	v_pk_mul_f32 v[80:81], v[86:87], v[80:81]
	v_pk_mul_f32 v[84:85], v[138:139], v[110:111] op_sel_hi:[0,1]
	v_pk_mul_f32 v[78:79], v[84:85], v[78:79]
	v_pk_mul_f32 v[84:85], v[138:139], v[106:107] op_sel_hi:[0,1]
	v_pk_mul_f32 v[86:87], v[138:139], v[108:109] op_sel_hi:[0,1]
	v_pk_mul_f32 v[86:87], v[86:87], v[76:77]
	v_pk_mul_f32 v[76:77], v[84:85], v[74:75]
	v_add_u32_e32 v82, 0x1e0000, v151
	v_cvt_pk_bf16_f32 v74, v78, v79
	v_cvt_pk_bf16_f32 v75, v80, v81
	v_cvt_pk_bf16_f32 v76, v76, v77
	v_cvt_pk_bf16_f32 v77, v86, v87
	buffer_store_dwordx4 v[74:77], v82, s[36:39], 0 offen nt
	v_pk_mul_f32 v[78:79], v[112:113], v[0:1] op_sel_hi:[1,0]
	v_cvt_f32_i32_e32 v51, v51
	v_pk_mul_f32 v[76:77], v[110:111], v[0:1] op_sel_hi:[1,0]
	v_pk_mul_f32 v[72:73], v[78:79], v[72:73]
	v_pk_mul_f32 v[70:71], v[76:77], v[70:71]
	v_pk_mul_f32 v[76:77], v[0:1], v[106:107] op_sel_hi:[0,1]
	v_pk_mul_f32 v[78:79], v[0:1], v[108:109] op_sel_hi:[0,1]
	v_add_u32_e32 v74, 0x210000, v151
	v_pk_mul_f32 v[78:79], v[78:79], v[68:69]
	v_pk_mul_f32 v[68:69], v[76:77], v[66:67]
	v_cvt_pk_bf16_f32 v66, v70, v71
	v_cvt_pk_bf16_f32 v67, v72, v73
	v_cvt_f32_i32_e32 v50, v50
	v_cvt_pk_bf16_f32 v68, v68, v69
	v_cvt_pk_bf16_f32 v69, v78, v79
	buffer_store_dwordx4 v[66:69], v74, s[36:39], 0 offen nt
	global_load_dwordx4 v[66:69], v[152:153], off offset:528
	s_nop 0
	global_load_dwordx4 v[70:73], v[152:153], off offset:512
	v_cvt_f32_i32_e32 v53, v53
	v_cvt_f32_i32_e32 v52, v52
	v_cvt_f32_i32_e32 v47, v47
	v_cvt_f32_i32_e32 v46, v46
	v_cvt_f32_i32_e32 v49, v49
	v_cvt_f32_i32_e32 v48, v48
	v_cvt_f32_i32_e32 v43, v43
	v_cvt_f32_i32_e32 v42, v42
	v_cvt_f32_i32_e32 v45, v45
	v_cvt_f32_i32_e32 v44, v44
	v_cvt_f32_i32_e32 v39, v39
	v_cvt_f32_i32_e32 v38, v38
	v_cvt_f32_i32_e32 v41, v41
	v_cvt_f32_i32_e32 v40, v40
	v_cvt_f32_i32_e32 v35, v35
	v_cvt_f32_i32_e32 v34, v34
	v_cvt_f32_i32_e32 v37, v37
	v_cvt_f32_i32_e32 v36, v36
	v_cvt_f32_i32_e32 v31, v31
	v_cvt_f32_i32_e32 v30, v30
	v_cvt_f32_i32_e32 v33, v33
	v_cvt_f32_i32_e32 v32, v32
	v_cvt_f32_i32_e32 v27, v27
	v_cvt_f32_i32_e32 v26, v26
	v_cvt_f32_i32_e32 v29, v29
	v_cvt_f32_i32_e32 v28, v28
	v_cvt_f32_i32_e32 v23, v23
	v_cvt_f32_i32_e32 v22, v22
	v_cvt_f32_i32_e32 v25, v25
	v_cvt_f32_i32_e32 v24, v24
	v_cvt_f32_i32_e32 v19, v19
	v_cvt_f32_i32_e32 v18, v18
	v_cvt_f32_i32_e32 v21, v21
	v_cvt_f32_i32_e32 v20, v20
	v_cvt_f32_i32_e32 v15, v15
	v_cvt_f32_i32_e32 v14, v14
	v_cvt_f32_i32_e32 v17, v17
	v_cvt_f32_i32_e32 v16, v16
	v_cvt_f32_i32_e32 v11, v11
	v_cvt_f32_i32_e32 v10, v10
	v_cvt_f32_i32_e32 v13, v13
	v_cvt_f32_i32_e32 v12, v12
	v_cvt_f32_i32_e32 v7, v7
	v_cvt_f32_i32_e32 v6, v6
	v_cvt_f32_i32_e32 v9, v9
	v_cvt_f32_i32_e32 v8, v8
	v_cvt_f32_i32_e32 v3, v3
	v_cvt_f32_i32_e32 v2, v2
	v_cvt_f32_i32_e32 v5, v5
	v_cvt_f32_i32_e32 v4, v4
	s_mov_b64 s[22:23], -1
	s_andn2_b64 vcc, exec, s[0:1]
	s_mov_b64 s[78:79], 0x6b600000
	s_mov_b32 s76, s90
	s_waitcnt vmcnt(0)
; __device__ __forceinline__ unsigned cvt_pk_bf16(float lo, float hi) { unsigned r; asm volatile("v_cvt_pk_bf16_f32 %0, %1, %2" : "=v"(r) : "v"(lo), "v"(hi)); return r; }
; #define PG8_BAR __builtin_amdgcn_s_barrier()
; template <class Epi, class Sched, bool ALIGN_EPI = false, bool SP2 = false, bool FP8 = false>
; __device__ __forceinline__ void gemm_phase(PG8_LAS unsigned char* lds, const Gemm g, const Sched& S, const Epi& E, const int tid_in) {
;     ...
;         cur = nxt; cA = nA; cB = nB; ++ui;
;         if constexpr (ALIGN_EPI) { if (wr == 1) PG8_BAR; }
;     __device__ __forceinline__ void operator()(const pg8::f32x4 (&acc)[2][2][4][2], const pg8::Unit& u, int wr, int wc, int fr_, int fq_) const {
;     ...
;         for (int bj = 0; bj < 2; ++bj) {
;             const pg8::f32x4 s0 = *(const pg8::f32x4*)(SW + col0 + bj * 128), s1 = *(const pg8::f32x4*)(SW + col0 + bj * 128 + 4);
; #pragma unroll
;             for (int ai = 0; ai < 2; ++ai)
; #pragma unroll
;                 for (int m = 0; m < 4; ++m) { const int row = row0 + ai * 128 + m * 16; const float sx = sxv[ai * 4 + m];
;                     const unsigned ro = (unsigned)(((size_t)row * ldc + col0) * 2);
;                     const pg8::f32x4 a0 = acc[ai][bj][m][0], a1 = acc[ai][bj][m][1];
;                     typedef int i32x4_ __attribute__((ext_vector_type(4)));
;                     const pg8::f32x4 f0 = __builtin_convertvector(__builtin_bit_cast(i32x4_, a0), pg8::f32x4) * (s0 * sx), f1 = __builtin_convertvector(__builtin_bit_cast(i32x4_, a1), pg8::f32x4) * (s1 * sx);
;                     const float v[8] = {f0[0], f0[1], f0[2], f0[3], f1[0], f1[1], f1[2], f1[3]};
;                     v4u w; w.x = pg8::cvt_pk_bf16(v[0], v[1]); w.y = pg8::cvt_pk_bf16(v[2], v[3]); w.z = pg8::cvt_pk_bf16(v[4], v[5]); w.w = pg8::cvt_pk_bf16(v[6], v[7]);
;                     __builtin_amdgcn_raw_buffer_store_b128(w, rs, ro + bj * 256, 0, 0); }
	v_pk_mul_f32 v[76:77], v[150:151], v[70:71] op_sel_hi:[0,1]
	v_pk_mul_f32 v[78:79], v[150:151], v[72:73] op_sel_hi:[0,1]
	v_pk_mul_f32 v[64:65], v[78:79], v[64:65]
	v_pk_mul_f32 v[62:63], v[76:77], v[62:63]
	v_pk_mul_f32 v[76:77], v[150:151], v[66:67] op_sel_hi:[0,1]
	v_pk_mul_f32 v[78:79], v[150:151], v[68:69] op_sel_hi:[0,1]
	v_pk_mul_f32 v[78:79], v[78:79], v[60:61]
	v_pk_mul_f32 v[60:61], v[76:77], v[58:59]
	v_cvt_pk_bf16_f32 v58, v62, v63
	v_cvt_pk_bf16_f32 v59, v64, v65
	s_nop 0
	v_cvt_pk_bf16_f32 v60, v60, v61
	v_cvt_pk_bf16_f32 v61, v78, v79
	buffer_store_dwordx4 v[58:61], v151, s[36:39], 0 offen offset:256 nt
	s_nop 1
	v_pk_mul_f32 v[58:59], v[148:149], v[70:71] op_sel_hi:[0,1]
	v_pk_mul_f32 v[60:61], v[148:149], v[72:73] op_sel_hi:[0,1]
	v_pk_mul_f32 v[56:57], v[60:61], v[56:57]
	v_pk_mul_f32 v[54:55], v[58:59], v[54:55]
	v_pk_mul_f32 v[58:59], v[148:149], v[66:67] op_sel_hi:[0,1]
	v_pk_mul_f32 v[60:61], v[148:149], v[68:69] op_sel_hi:[0,1]
	v_pk_mul_f32 v[60:61], v[60:61], v[52:53]
	v_pk_mul_f32 v[52:53], v[58:59], v[50:51]
	v_cvt_pk_bf16_f32 v50, v54, v55
	v_cvt_pk_bf16_f32 v51, v56, v57
	s_nop 0
	v_cvt_pk_bf16_f32 v52, v52, v53
	v_cvt_pk_bf16_f32 v53, v60, v61
	buffer_store_dwordx4 v[50:53], v130, s[36:39], 0 offen offset:256 nt
	s_nop 1
	v_pk_mul_f32 v[50:51], v[146:147], v[70:71] op_sel_hi:[0,1]
	v_pk_mul_f32 v[52:53], v[146:147], v[72:73] op_sel_hi:[0,1]
	v_pk_mul_f32 v[48:49], v[52:53], v[48:49]
	v_pk_mul_f32 v[46:47], v[50:51], v[46:47]
	v_pk_mul_f32 v[50:51], v[146:147], v[66:67] op_sel_hi:[0,1]
	v_pk_mul_f32 v[52:53], v[146:147], v[68:69] op_sel_hi:[0,1]
	v_pk_mul_f32 v[52:53], v[52:53], v[44:45]
	v_pk_mul_f32 v[44:45], v[50:51], v[42:43]
	v_cvt_pk_bf16_f32 v42, v46, v47
	v_cvt_pk_bf16_f32 v43, v48, v49
	s_nop 0
	v_cvt_pk_bf16_f32 v44, v44, v45
	v_cvt_pk_bf16_f32 v45, v52, v53
	buffer_store_dwordx4 v[42:45], v122, s[36:39], 0 offen offset:256 nt
	s_nop 1
	v_pk_mul_f32 v[42:43], v[144:145], v[70:71] op_sel_hi:[0,1]
	v_pk_mul_f32 v[44:45], v[144:145], v[72:73] op_sel_hi:[0,1]
	v_pk_mul_f32 v[40:41], v[44:45], v[40:41]
	v_pk_mul_f32 v[38:39], v[42:43], v[38:39]
	v_pk_mul_f32 v[42:43], v[144:145], v[66:67] op_sel_hi:[0,1]
	v_pk_mul_f32 v[44:45], v[144:145], v[68:69] op_sel_hi:[0,1]
	v_pk_mul_f32 v[44:45], v[44:45], v[36:37]
	v_pk_mul_f32 v[36:37], v[42:43], v[34:35]
	v_cvt_pk_bf16_f32 v34, v38, v39
	v_cvt_pk_bf16_f32 v35, v40, v41
	s_nop 0
	v_cvt_pk_bf16_f32 v36, v36, v37
	v_cvt_pk_bf16_f32 v37, v44, v45
	buffer_store_dwordx4 v[34:37], v114, s[36:39], 0 offen offset:256 nt
	s_nop 1
	v_pk_mul_f32 v[34:35], v[142:143], v[70:71] op_sel_hi:[0,1]
	v_pk_mul_f32 v[36:37], v[142:143], v[72:73] op_sel_hi:[0,1]
	v_pk_mul_f32 v[32:33], v[36:37], v[32:33]
	v_pk_mul_f32 v[30:31], v[34:35], v[30:31]
	v_pk_mul_f32 v[34:35], v[142:143], v[66:67] op_sel_hi:[0,1]
	v_pk_mul_f32 v[36:37], v[142:143], v[68:69] op_sel_hi:[0,1]
	v_pk_mul_f32 v[36:37], v[36:37], v[28:29]
	v_pk_mul_f32 v[28:29], v[34:35], v[26:27]
	v_cvt_pk_bf16_f32 v26, v30, v31
	v_cvt_pk_bf16_f32 v27, v32, v33
	s_nop 0
	v_cvt_pk_bf16_f32 v28, v28, v29
	v_cvt_pk_bf16_f32 v29, v36, v37
	buffer_store_dwordx4 v[26:29], v98, s[36:39], 0 offen offset:256 nt
	s_nop 1
	v_pk_mul_f32 v[26:27], v[140:141], v[70:71] op_sel_hi:[0,1]
	v_pk_mul_f32 v[28:29], v[140:141], v[72:73] op_sel_hi:[0,1]
	v_pk_mul_f32 v[24:25], v[28:29], v[24:25]
	v_pk_mul_f32 v[22:23], v[26:27], v[22:23]
	v_pk_mul_f32 v[26:27], v[140:141], v[66:67] op_sel_hi:[0,1]
	v_pk_mul_f32 v[28:29], v[140:141], v[68:69] op_sel_hi:[0,1]
	v_pk_mul_f32 v[28:29], v[28:29], v[20:21]
	v_pk_mul_f32 v[20:21], v[26:27], v[18:19]
	v_cvt_pk_bf16_f32 v18, v22, v23
	v_cvt_pk_bf16_f32 v19, v24, v25
	s_nop 0
	v_cvt_pk_bf16_f32 v20, v20, v21
	v_cvt_pk_bf16_f32 v21, v28, v29
	buffer_store_dwordx4 v[18:21], v90, s[36:39], 0 offen offset:256 nt
	s_nop 1
	v_pk_mul_f32 v[18:19], v[138:139], v[70:71] op_sel_hi:[0,1]
	v_pk_mul_f32 v[20:21], v[138:139], v[72:73] op_sel_hi:[0,1]
	v_pk_mul_f32 v[16:17], v[20:21], v[16:17]
	v_pk_mul_f32 v[14:15], v[18:19], v[14:15]
	v_pk_mul_f32 v[18:19], v[138:139], v[66:67] op_sel_hi:[0,1]
	v_pk_mul_f32 v[20:21], v[138:139], v[68:69] op_sel_hi:[0,1]
	v_pk_mul_f32 v[20:21], v[20:21], v[12:13]
	v_pk_mul_f32 v[12:13], v[18:19], v[10:11]
	v_cvt_pk_bf16_f32 v10, v14, v15
	v_cvt_pk_bf16_f32 v11, v16, v17
	s_nop 0
	v_cvt_pk_bf16_f32 v12, v12, v13
	v_cvt_pk_bf16_f32 v13, v20, v21
	buffer_store_dwordx4 v[10:13], v82, s[36:39], 0 offen offset:256 nt
	s_nop 1
	v_pk_mul_f32 v[10:11], v[0:1], v[70:71] op_sel_hi:[0,1]
	v_pk_mul_f32 v[12:13], v[0:1], v[72:73] op_sel_hi:[0,1]
	v_pk_mul_f32 v[8:9], v[12:13], v[8:9]
	v_pk_mul_f32 v[6:7], v[10:11], v[6:7]
	v_pk_mul_f32 v[10:11], v[0:1], v[66:67] op_sel_hi:[0,1]
	v_pk_mul_f32 v[12:13], v[0:1], v[68:69] op_sel_hi:[0,1]
	v_pk_mul_f32 v[12:13], v[12:13], v[4:5]
	v_pk_mul_f32 v[4:5], v[10:11], v[2:3]
	v_cvt_pk_bf16_f32 v2, v6, v7
	v_cvt_pk_bf16_f32 v3, v8, v9
	s_nop 0
	v_cvt_pk_bf16_f32 v4, v4, v5
	v_cvt_pk_bf16_f32 v5, v12, v13
	buffer_store_dwordx4 v[2:5], v74, s[36:39], 0 offen offset:256 nt
	s_cbranch_vccnz .LBB0_281
	s_nop 0
	v_mov_b32_e32 v2, v1
	s_andn2_b64 vcc, exec, s[6:7]
	s_cbranch_vccnz .LBB0_280
	s_barrier
	s_branch .LBB0_280
